# four barriers per unit (one more between the row max and the exponentials), the two units of a workgroup half a unit apart
# baseline (speedup 1.0000x reference)
.LBB0_471:
	v_cndmask_b32_e64 v70, v81, v226, s[78:79]
	v_max3_f32 v33, v18, v97, v20
	v_max3_f32 v33, v33, v19, v22
	v_max3_f32 v33, v33, v21, v24
	v_max3_f32 v33, v33, v23, v26
	v_max3_f32 v33, v33, v25, v28
	v_max3_f32 v33, v33, v27, v31
	v_max3_f32 v33, v33, v29, v30
	v_max3_f32 v33, v33, v32, v3
	v_max3_f32 v33, v33, v2, v5
	v_max3_f32 v33, v33, v4, v7
	v_max3_f32 v33, v33, v6, v9
	v_max3_f32 v33, v33, v8, v11
	v_max3_f32 v33, v33, v10, v13
	v_max3_f32 v33, v33, v12, v15
	v_max3_f32 v33, v33, v14, v17
	v_max3_f32 v33, v33, v16, v35
	v_max3_f32 v33, v33, v34, v37
	v_max3_f32 v33, v33, v36, v39
	v_max3_f32 v33, v33, v38, v41
	v_max3_f32 v33, v33, v40, v43
	v_max3_f32 v33, v33, v42, v45
	v_max3_f32 v33, v33, v44, v47
	v_max3_f32 v33, v33, v46, v49
	v_max3_f32 v33, v33, v48, v51
	v_max3_f32 v33, v33, v50, v53
	v_max3_f32 v33, v33, v52, v55
	v_max3_f32 v33, v33, v54, v57
	v_max3_f32 v33, v33, v56, v59
	v_max3_f32 v33, v33, v58, v61
	v_max3_f32 v33, v33, v60, v63
	v_max3_f32 v33, v33, v62, v65
	v_max3_f32 v33, v33, v64, v83
	v_max3_f32 v33, v33, v82, v85
	v_max3_f32 v33, v33, v84, v87
	v_max3_f32 v33, v33, v86, v89
	v_max3_f32 v33, v33, v88, v91
	v_max3_f32 v33, v33, v90, v93
	v_max3_f32 v33, v33, v92, v95
	v_max3_f32 v33, v33, v94, v70
	v_max_f32_e32 v33, v33, v96
	v_and_b32_e32 v67, 64, v209
	v_xor_b32_e32 v66, 32, v209
	v_add_u32_e32 v67, 64, v67
	v_cmp_lt_i32_e32 vcc, v66, v67
	s_nop 1
	v_cndmask_b32_e32 v66, v209, v66, vcc
	v_lshlrev_b32_e32 v118, 2, v66
	ds_bpermute_b32 v66, v118, v33
	s_waitcnt lgkmcnt(0)
	v_max_f32_e32 v66, v33, v66
	s_barrier
	v_pk_add_f32 v[2:3], v[2:3], v[66:67] op_sel_hi:[1,0] neg_lo:[0,1] neg_hi:[0,1]
	v_pk_add_f32 v[4:5], v[4:5], v[66:67] op_sel_hi:[1,0] neg_lo:[0,1] neg_hi:[0,1]
	v_pk_add_f32 v[6:7], v[6:7], v[66:67] op_sel_hi:[1,0] neg_lo:[0,1] neg_hi:[0,1]
	v_pk_add_f32 v[8:9], v[8:9], v[66:67] op_sel_hi:[1,0] neg_lo:[0,1] neg_hi:[0,1]
	v_pk_add_f32 v[10:11], v[10:11], v[66:67] op_sel_hi:[1,0] neg_lo:[0,1] neg_hi:[0,1]
	v_pk_add_f32 v[12:13], v[12:13], v[66:67] op_sel_hi:[1,0] neg_lo:[0,1] neg_hi:[0,1]
	v_pk_add_f32 v[14:15], v[14:15], v[66:67] op_sel_hi:[1,0] neg_lo:[0,1] neg_hi:[0,1]
	v_pk_add_f32 v[16:17], v[16:17], v[66:67] op_sel_hi:[1,0] neg_lo:[0,1] neg_hi:[0,1]
	v_pk_add_f32 v[18:19], v[18:19], v[66:67] op_sel_hi:[1,0] neg_lo:[0,1] neg_hi:[0,1]
	v_pk_add_f32 v[20:21], v[20:21], v[66:67] op_sel_hi:[1,0] neg_lo:[0,1] neg_hi:[0,1]
	v_pk_add_f32 v[22:23], v[22:23], v[66:67] op_sel_hi:[1,0] neg_lo:[0,1] neg_hi:[0,1]
	v_pk_add_f32 v[24:25], v[24:25], v[66:67] op_sel_hi:[1,0] neg_lo:[0,1] neg_hi:[0,1]
	v_pk_add_f32 v[26:27], v[26:27], v[66:67] op_sel_hi:[1,0] neg_lo:[0,1] neg_hi:[0,1]
	v_pk_add_f32 v[28:29], v[28:29], v[66:67] op_sel_hi:[1,0] neg_lo:[0,1] neg_hi:[0,1]
	v_pk_add_f32 v[30:31], v[30:31], v[66:67] op_sel_hi:[1,0] neg_lo:[0,1] neg_hi:[0,1]
	v_pk_add_f32 v[34:35], v[34:35], v[66:67] op_sel_hi:[1,0] neg_lo:[0,1] neg_hi:[0,1]
	v_pk_add_f32 v[36:37], v[36:37], v[66:67] op_sel_hi:[1,0] neg_lo:[0,1] neg_hi:[0,1]
	v_pk_add_f32 v[38:39], v[38:39], v[66:67] op_sel_hi:[1,0] neg_lo:[0,1] neg_hi:[0,1]
	v_pk_add_f32 v[40:41], v[40:41], v[66:67] op_sel_hi:[1,0] neg_lo:[0,1] neg_hi:[0,1]
	v_pk_add_f32 v[42:43], v[42:43], v[66:67] op_sel_hi:[1,0] neg_lo:[0,1] neg_hi:[0,1]
	v_pk_add_f32 v[44:45], v[44:45], v[66:67] op_sel_hi:[1,0] neg_lo:[0,1] neg_hi:[0,1]
	v_pk_add_f32 v[46:47], v[46:47], v[66:67] op_sel_hi:[1,0] neg_lo:[0,1] neg_hi:[0,1]
	v_pk_add_f32 v[48:49], v[48:49], v[66:67] op_sel_hi:[1,0] neg_lo:[0,1] neg_hi:[0,1]
	v_pk_add_f32 v[50:51], v[50:51], v[66:67] op_sel_hi:[1,0] neg_lo:[0,1] neg_hi:[0,1]
	v_pk_add_f32 v[52:53], v[52:53], v[66:67] op_sel_hi:[1,0] neg_lo:[0,1] neg_hi:[0,1]
	v_pk_add_f32 v[54:55], v[54:55], v[66:67] op_sel_hi:[1,0] neg_lo:[0,1] neg_hi:[0,1]
	v_pk_add_f32 v[56:57], v[56:57], v[66:67] op_sel_hi:[1,0] neg_lo:[0,1] neg_hi:[0,1]
	v_pk_add_f32 v[58:59], v[58:59], v[66:67] op_sel_hi:[1,0] neg_lo:[0,1] neg_hi:[0,1]
	v_pk_add_f32 v[60:61], v[60:61], v[66:67] op_sel_hi:[1,0] neg_lo:[0,1] neg_hi:[0,1]
	v_pk_add_f32 v[62:63], v[62:63], v[66:67] op_sel_hi:[1,0] neg_lo:[0,1] neg_hi:[0,1]
	v_pk_add_f32 v[64:65], v[64:65], v[66:67] op_sel_hi:[1,0] neg_lo:[0,1] neg_hi:[0,1]
	v_pk_add_f32 v[82:83], v[82:83], v[66:67] op_sel_hi:[1,0] neg_lo:[0,1] neg_hi:[0,1]
	v_pk_add_f32 v[84:85], v[84:85], v[66:67] op_sel_hi:[1,0] neg_lo:[0,1] neg_hi:[0,1]
	v_pk_add_f32 v[86:87], v[86:87], v[66:67] op_sel_hi:[1,0] neg_lo:[0,1] neg_hi:[0,1]
	v_pk_add_f32 v[88:89], v[88:89], v[66:67] op_sel_hi:[1,0] neg_lo:[0,1] neg_hi:[0,1]
	v_pk_add_f32 v[90:91], v[90:91], v[66:67] op_sel_hi:[1,0] neg_lo:[0,1] neg_hi:[0,1]
	v_pk_add_f32 v[92:93], v[92:93], v[66:67] op_sel_hi:[1,0] neg_lo:[0,1] neg_hi:[0,1]
	v_pk_add_f32 v[94:95], v[94:95], v[66:67] op_sel_hi:[1,0] neg_lo:[0,1] neg_hi:[0,1]
	v_pk_add_f32 v[96:97], v[96:97], v[66:67] op_sel_hi:[1,0] neg_lo:[0,1] neg_hi:[0,1]
	v_sub_f32_e32 v32, v32, v66
	v_sub_f32_e32 v70, v70, v66
	v_exp_f32_e32 v33, v97
	v_exp_f32_e32 v18, v18
	v_exp_f32_e32 v19, v19
	v_exp_f32_e32 v20, v20
	v_mov_b32_e32 v244, 0
	v_mov_b32_e32 v245, 0
	v_add_f32_e32 v244, v33, v244
	v_exp_f32_e32 v21, v21
	v_exp_f32_e32 v22, v22
	v_pk_add_f32 v[244:245], v[18:19], v[244:245]
	v_exp_f32_e32 v23, v23
	v_exp_f32_e32 v24, v24
	v_pk_add_f32 v[244:245], v[20:21], v[244:245]
	v_exp_f32_e32 v119, v25
	v_exp_f32_e32 v120, v26
	v_pk_add_f32 v[244:245], v[22:23], v[244:245]
	v_exp_f32_e32 v121, v27
	v_add_f32_e32 v244, v24, v244
	v_exp_f32_e32 v122, v28
	v_add_f32_e32 v244, v119, v244
	v_exp_f32_e32 v123, v29
	v_exp_f32_e32 v124, v31
	v_pk_add_f32 v[244:245], v[120:121], v[244:245]
	v_exp_f32_e32 v125, v32
	v_exp_f32_e32 v126, v30
	v_pk_add_f32 v[244:245], v[122:123], v[244:245]
	v_exp_f32_e32 v103, v2
	v_exp_f32_e32 v106, v3
	v_pk_add_f32 v[244:245], v[124:125], v[244:245]
	v_exp_f32_e32 v107, v4
	v_add_f32_e32 v244, v126, v244
	v_exp_f32_e32 v110, v5
	v_exp_f32_e32 v111, v6
	v_exp_f32_e32 v114, v7
	v_pk_add_f32 v[244:245], v[106:107], v[244:245]
	v_exp_f32_e32 v115, v8
	v_exp_f32_e32 v117, v9
	v_pk_add_f32 v[244:245], v[110:111], v[244:245]
	v_exp_f32_e32 v102, v10
	v_exp_f32_e32 v104, v11
	v_pk_add_f32 v[244:245], v[114:115], v[244:245]
	v_exp_f32_e32 v105, v12
	v_exp_f32_e32 v108, v13
	v_pk_add_f32 v[244:245], v[102:103], v[244:245]
	v_exp_f32_e32 v109, v14
	v_exp_f32_e32 v112, v15
	v_pk_add_f32 v[244:245], v[104:105], v[244:245]
	v_exp_f32_e32 v113, v16
	v_exp_f32_e32 v116, v17
	v_pk_add_f32 v[244:245], v[108:109], v[244:245]
	v_exp_f32_e32 v72, v34
	v_exp_f32_e32 v75, v35
	v_pk_add_f32 v[244:245], v[112:113], v[244:245]
	v_exp_f32_e32 v76, v36
	v_pk_add_f32 v[244:245], v[116:117], v[244:245]
	v_exp_f32_e32 v79, v37
	v_exp_f32_e32 v80, v38
	v_exp_f32_e32 v98, v39
	v_exp_f32_e32 v99, v40
	v_exp_f32_e32 v101, v41
	v_exp_f32_e32 v71, v42
	v_exp_f32_e32 v73, v43
	v_pk_add_f32 v[244:245], v[98:99], v[244:245]
	v_exp_f32_e32 v74, v44
	v_exp_f32_e32 v77, v45
	v_exp_f32_e32 v78, v46
	v_pk_add_f32 v[244:245], v[72:73], v[244:245]
	v_exp_f32_e32 v81, v47
	v_pk_add_f32 v[244:245], v[74:75], v[244:245]
	v_exp_f32_e32 v97, v48
	v_pk_add_f32 v[244:245], v[76:77], v[244:245]
	v_exp_f32_e32 v100, v49
	v_pk_add_f32 v[244:245], v[78:79], v[244:245]
	v_exp_f32_e32 v41, v50
	v_pk_add_f32 v[244:245], v[80:81], v[244:245]
	v_exp_f32_e32 v46, v51
	v_add_f32_e32 v244, v97, v244
	v_exp_f32_e32 v47, v52
	v_pk_add_f32 v[244:245], v[100:101], v[244:245]
	v_exp_f32_e32 v53, v53
	v_exp_f32_e32 v54, v54
	v_exp_f32_e32 v67, v55
	v_pk_add_f32 v[244:245], v[46:47], v[244:245]
	v_exp_f32_e32 v68, v56
	v_exp_f32_e32 v69, v57
	v_exp_f32_e32 v38, v58
	v_add_f32_e32 v244, v67, v244
	v_exp_f32_e32 v44, v59
	v_exp_f32_e32 v45, v60
	v_pk_add_f32 v[244:245], v[68:69], v[244:245]
	v_exp_f32_e32 v51, v61
	v_exp_f32_e32 v52, v62
	v_exp_f32_e32 v57, v63
	v_pk_add_f32 v[244:245], v[44:45], v[244:245]
	v_exp_f32_e32 v58, v64
	v_exp_f32_e32 v62, v65
	v_pk_add_f32 v[244:245], v[52:53], v[244:245]
	v_exp_f32_e32 v37, v82
	v_exp_f32_e32 v42, v83
	v_add_f32_e32 v244, v58, v244
	v_exp_f32_e32 v43, v84
	v_exp_f32_e32 v49, v85
	v_exp_f32_e32 v50, v86
	v_exp_f32_e32 v55, v87
	v_pk_add_f32 v[244:245], v[42:43], v[244:245]
	v_exp_f32_e32 v56, v88
	v_exp_f32_e32 v61, v89
	v_pk_add_f32 v[244:245], v[50:51], v[244:245]
	v_exp_f32_e32 v36, v90
	v_pk_add_f32 v[244:245], v[54:55], v[244:245]
	v_exp_f32_e32 v39, v91
	v_pk_add_f32 v[244:245], v[56:57], v[244:245]
	v_exp_f32_e32 v40, v92
	v_add_f32_e32 v244, v61, v244
	v_pk_add_f32 v[244:245], v[36:37], v[244:245]
	v_pk_add_f32 v[244:245], v[38:39], v[244:245]
	v_pk_add_f32 v[244:245], v[40:41], v[244:245]
	v_exp_f32_e32 v48, v93
	v_cvt_pk_bf16_f32 v2, v33, v18
	v_cvt_pk_bf16_f32 v3, v19, v20
	v_cvt_pk_bf16_f32 v4, v21, v22
	v_cvt_pk_bf16_f32 v5, v23, v24
	s_bitcmp1_b32 s96, 0
	s_cbranch_scc1 .Latt_b3m
	s_waitcnt vmcnt(0)
